# P14 next-row loads issued at the top of the iteration into spare registers with a counted wait at the tail; P6 K fragments 4..6 loaded with the others at the loop head
# speedup vs baseline: 1.0091x; 1.0071x over previous
.LBB0_1664:
	v_add_u32_e32 v138, s62, v66
	v_lshlrev_b64 v[66:67], 13, v[138:139]
	v_lshl_add_u64 v[132:133], v[140:141], 0, v[66:67]
	v_lshl_add_u64 v[130:131], v[142:143], 0, v[66:67]
	global_load_dwordx4 v[66:69], v[132:133], off
	global_load_dwordx4 v[114:117], v[132:133], off offset:1024
	global_load_dwordx4 v[122:125], v[132:133], off offset:2048
	v_add_co_u32_e32 v180, vcc, s49, v130
	global_load_dwordx4 v[126:129], v[132:133], off offset:3072
	global_load_dwordx4 v[168:171], v[130:131], off
	global_load_dwordx4 v[118:121], v[130:131], off offset:1024
	global_load_dwordx4 v[134:137], v[130:131], off offset:2048
	s_mov_b64 s[42:43], vcc
	v_add_co_u32_e32 v132, vcc, s49, v132
	v_add_f32_e32 v149, 0, v147
	s_nop 0
	v_addc_co_u32_e32 v133, vcc, 0, v133, vcc
	global_load_dwordx4 v[172:175], v[132:133], off offset:3072
	global_load_dwordx4 v[206:209], v[132:133], off
	global_load_dwordx4 v[210:213], v[132:133], off offset:1024
	global_load_dwordx4 v[214:217], v[132:133], off offset:2048
	v_addc_co_u32_e64 v181, vcc, 0, v131, s[42:43]
	s_add_i32 s63, s63, -1
	s_waitcnt vmcnt(10)
	v_mfma_f32_32x32x16_bf16 v[66:81], v[66:69], v[82:85], 0
	s_waitcnt vmcnt(9)
	v_mfma_f32_32x32x16_bf16 v[66:81], v[114:117], v[86:89], v[66:81]
	s_waitcnt vmcnt(8)
	v_mfma_f32_32x32x16_bf16 v[66:81], v[122:125], v[90:93], v[66:81]
	s_waitcnt vmcnt(7)
	v_mfma_f32_32x32x16_bf16 v[66:81], v[126:129], v[94:97], v[66:81]
	s_waitcnt vmcnt(2)
	v_mfma_f32_32x32x16_bf16 v[66:81], v[206:209], v[98:101], v[66:81]
	s_waitcnt vmcnt(1)
	v_mfma_f32_32x32x16_bf16 v[66:81], v[210:213], v[102:105], v[66:81]
	global_load_dwordx4 v[122:125], v[130:131], off offset:3072
	s_waitcnt vmcnt(1)
	v_mfma_f32_32x32x16_bf16 v[66:81], v[214:217], v[106:109], v[66:81]
	global_load_dwordx4 v[176:179], v[180:181], off
	global_load_dwordx4 v[126:129], v[180:181], off offset:1024
	global_load_dwordx4 v[130:133], v[180:181], off offset:2048
	global_load_dwordx4 v[114:117], v[180:181], off offset:3072
	v_mfma_f32_32x32x16_bf16 v[66:81], v[172:175], v[110:113], v[66:81]
	s_nop 11
	v_mul_f32_e32 v180, 0x3e0293ee, v75
	v_mul_f32_e32 v76, 0x3e0293ee, v76
	v_mul_f32_e32 v75, 0x3e0293ee, v77
	v_mul_f32_e32 v78, 0x3e0293ee, v78
	v_mul_f32_e32 v182, 0x3e0293ee, v79
	v_mul_f32_e32 v80, 0x3e0293ee, v80
	v_mul_f32_e32 v79, 0x3e0293ee, v81
	v_mul_f32_e32 v66, 0x3e0293ee, v66
	v_mul_f32_e32 v172, 0x3e0293ee, v67
	v_mul_f32_e32 v68, 0x3e0293ee, v68
	v_mul_f32_e32 v67, 0x3e0293ee, v69
	v_mul_f32_e32 v70, 0x3e0293ee, v70
	v_mul_f32_e32 v174, 0x3e0293ee, v71
	v_mul_f32_e32 v72, 0x3e0293ee, v72
	v_mul_f32_e32 v71, 0x3e0293ee, v73
	v_mul_f32_e32 v74, 0x3e0293ee, v74
	v_exp_f32_e64 v201, -|v180|
	v_exp_f32_e64 v202, -|v76|
	v_exp_f32_e64 v203, -|v75|
	v_max_f32_e32 v195, 0, v75
	v_exp_f32_e64 v75, -|v78|
	v_exp_f32_e64 v204, -|v182|
	v_exp_f32_e64 v205, -|v80|
	v_exp_f32_e64 v206, -|v79|
	v_exp_f32_e64 v138, -|v66|
	v_exp_f32_e64 v167, -|v172|
	v_exp_f32_e64 v173, -|v68|
	v_exp_f32_e64 v175, -|v67|
	v_max_f32_e32 v187, 0, v67
	v_exp_f32_e64 v67, -|v70|
	v_exp_f32_e64 v181, -|v174|
	v_exp_f32_e64 v183, -|v72|
	v_exp_f32_e64 v200, -|v71|
	v_max_f32_e32 v191, 0, v71
	v_exp_f32_e64 v71, -|v74|
	v_add_f32_e32 v209, 1.0, v201
	v_add_f32_e32 v211, 1.0, v202
	v_add_f32_e32 v212, 1.0, v203
	v_add_f32_e32 v75, 1.0, v75
	v_add_f32_e32 v213, 1.0, v204
	v_add_f32_e32 v215, 1.0, v205
	v_add_f32_e32 v216, 1.0, v206
	v_max_f32_e32 v199, 0, v79
	v_add_f32_e32 v79, 1.0, v138
	v_add_f32_e32 v138, 1.0, v167
	v_add_f32_e32 v167, 1.0, v173
	v_add_f32_e32 v173, 1.0, v175
	v_add_f32_e32 v67, 1.0, v67
	v_add_f32_e32 v175, 1.0, v181
	v_add_f32_e32 v181, 1.0, v183
	v_add_f32_e32 v183, 1.0, v200
	v_add_f32_e32 v71, 1.0, v71
	v_log_f32_e32 v210, v209
	v_log_f32_e32 v209, v211
	v_log_f32_e32 v211, v212
	v_log_f32_e32 v212, v75
	v_log_f32_e32 v214, v213
	v_log_f32_e32 v213, v215
	v_log_f32_e32 v215, v216
	v_log_f32_e32 v204, v67
	v_log_f32_e32 v206, v175
	v_log_f32_e32 v205, v181
	v_log_f32_e32 v207, v183
	v_log_f32_e32 v208, v71
	v_log_f32_e32 v202, v138
	v_log_f32_e32 v203, v173
	v_max_f32_e32 v196, 0, v78
	v_max_f32_e32 v198, 0, v182
	v_max_f32_e32 v197, 0, v80
	v_log_f32_e32 v200, v79
	v_log_f32_e32 v201, v167
	v_max_f32_e32 v188, 0, v70
	v_max_f32_e32 v190, 0, v174
	v_max_f32_e32 v189, 0, v72
	v_max_f32_e32 v192, 0, v74
	v_max_f32_e32 v194, 0, v180
	v_max_f32_e32 v193, 0, v76
	v_pk_add_f32 v[196:197], v[196:197], v[212:213]
	v_pk_add_f32 v[198:199], v[198:199], v[214:215]
	v_max_f32_e32 v186, 0, v172
	v_pk_add_f32 v[188:189], v[188:189], v[204:205]
	v_pk_add_f32 v[190:191], v[190:191], v[206:207]
	v_pk_add_f32 v[192:193], v[192:193], v[208:209]
	v_pk_add_f32 v[194:195], v[194:195], v[210:211]
	v_pk_add_f32 v[206:207], v[198:199], v[196:197] neg_lo:[1,1] neg_hi:[1,1]
	v_max_f32_e32 v184, 0, v66
	v_max_f32_e32 v185, 0, v68
	v_pk_add_f32 v[186:187], v[186:187], v[202:203]
	v_pk_add_f32 v[202:203], v[190:191], v[188:189] neg_lo:[1,1] neg_hi:[1,1]
	v_pk_add_f32 v[204:205], v[194:195], v[192:193] neg_lo:[1,1] neg_hi:[1,1]
	v_pk_add_f32 v[206:207], v[206:207], v[206:207] op_sel:[0,1] op_sel_hi:[1,0]
	v_pk_add_f32 v[184:185], v[184:185], v[200:201]
	v_pk_add_f32 v[202:203], v[202:203], v[202:203] op_sel:[0,1] op_sel_hi:[1,0]
	v_pk_add_f32 v[204:205], v[204:205], v[204:205] op_sel:[0,1] op_sel_hi:[1,0]
	v_mov_b32_e32 v219, v206
	v_pk_add_f32 v[200:201], v[186:187], v[184:185] neg_lo:[1,1] neg_hi:[1,1]
	v_mov_b32_e32 v75, v202
	v_mov_b32_e32 v218, v204
	v_permlane32_swap_b32_e32 v206, v219
	v_pk_add_f32 v[200:201], v[200:201], v[200:201] op_sel:[0,1] op_sel_hi:[1,0]
	v_permlane32_swap_b32_e32 v202, v75
	v_permlane32_swap_b32_e32 v204, v218
	v_mov_b32_e32 v205, v206
	v_add_f32_e32 v201, v202, v75
	v_pk_add_f32 v[202:203], v[204:205], v[218:219]
	v_fma_f32 v67, v69, s68, -v187
	v_fma_f32 v69, v73, s68, -v191
	v_fma_f32 v73, v81, s68, -v199
	v_mov_b32_e32 v216, v200
	v_cndmask_b32_e64 v81, 0, v219, s[6:7]
	v_pk_add_f32 v[204:205], v[202:203], v[202:203] op_sel:[0,1] op_sel_hi:[1,0]
	v_fma_f32 v71, v77, s68, -v195
	v_mov_b32_e32 v214, v197
	v_mov_b32_e32 v215, v199
	v_permlane32_swap_b32_e32 v200, v216
	v_cndmask_b32_e64 v77, 0, v218, s[6:7]
	v_add_f32_e32 v81, v149, v81
	v_add_f32_e32 v138, v147, v203
	v_mov_b32_e32 v217, v204
	v_cndmask_b32_e64 v75, 0, v75, s[6:7]
	v_pk_add_f32 v[202:203], v[80:81], v[214:215] neg_lo:[0,1] neg_hi:[0,1]
	v_add_f32_e32 v73, v73, v81
	v_add_f32_e32 v149, v147, v204
	v_add_f32_e32 v77, v77, v138
	v_pk_add_f32 v[80:81], v[200:201], v[216:217]
	v_mov_b32_e32 v210, v189
	v_mov_b32_e32 v211, v191
	v_mov_b32_e32 v212, v193
	v_mov_b32_e32 v213, v195
	v_cndmask_b32_e64 v79, 0, v216, s[6:7]
	v_exp_f32_e32 v138, v73
	v_add_f32_e32 v73, v75, v149
	v_add_f32_e32 v75, v71, v77
	v_add_f32_e32 v71, v147, v81
	v_mov_b32_e32 v208, v185
	v_mov_b32_e32 v209, v187
	v_pk_add_f32 v[200:201], v[76:77], v[212:213] neg_lo:[0,1] neg_hi:[0,1]
	v_pk_add_f32 v[76:77], v[72:73], v[210:211] neg_lo:[0,1] neg_hi:[0,1]
	v_add_f32_e32 v72, v69, v73
	v_add_f32_e32 v69, v79, v71
	v_mov_b32_e32 v191, v189
	v_mov_b32_e32 v175, v77
	v_add_f32_e32 v71, 0, v72
	v_add_f32_e32 v76, v76, v77
	v_pk_add_f32 v[72:73], v[68:69], v[208:209] neg_lo:[0,1] neg_hi:[0,1]
	v_mov_b32_e32 v187, v185
	v_add_f32_e32 v67, v67, v69
	v_pk_add_f32 v[68:69], v[174:175], v[190:191] neg_lo:[0,1] neg_hi:[0,1]
	v_add_f32_e32 v76, 0, v76
	v_mov_b32_e32 v173, v73
	v_exp_f32_e32 v77, v71
	v_add_f32_e32 v67, 0, v67
	v_add_f32_e32 v72, v72, v73
	v_mov_b32_e32 v71, v69
	v_exp_f32_e32 v73, v76
	v_add_f32_e32 v76, v68, v69
	v_pk_add_f32 v[68:69], v[172:173], v[186:187] neg_lo:[0,1] neg_hi:[0,1]
	v_mov_b32_e32 v185, v186
	v_exp_f32_e32 v79, v67
	v_mov_b32_e32 v67, v69
	v_mov_b32_e32 v189, v190
	v_pk_add_f32 v[66:67], v[66:67], v[184:185] neg_lo:[0,1] neg_hi:[0,1]
	v_pk_add_f32 v[70:71], v[70:71], v[188:189] neg_lo:[0,1] neg_hi:[0,1]
	v_add_f32_e32 v68, v68, v69
	v_add_f32_e32 v66, v66, v67
	v_add_f32_e32 v69, v70, v71
	v_add_f32_e32 v68, 0, v68
	v_add_f32_e32 v66, 0, v66
	v_add_f32_e32 v72, 0, v72
	v_add_f32_e32 v76, 0, v76
	v_add_f32_e32 v69, 0, v69
	v_exp_f32_e32 v70, v68
	v_exp_f32_e32 v66, v66
	v_exp_f32_e32 v72, v72
	v_exp_f32_e32 v76, v76
	v_exp_f32_e32 v68, v69
	v_mov_b32_e32 v199, v197
	v_mov_b32_e32 v183, v203
	v_mov_b32_e32 v195, v193
	v_cvt_pk_bf16_f32 v66, v66, v70
	v_pk_add_f32 v[70:71], v[182:183], v[198:199] neg_lo:[0,1] neg_hi:[0,1]
	v_mov_b32_e32 v181, v201
	v_mov_b32_e32 v197, v198
	v_cvt_pk_bf16_f32 v69, v73, v77
	v_cvt_pk_bf16_f32 v67, v72, v79
	v_cvt_pk_bf16_f32 v68, v68, v76
	v_add_f32_e32 v72, 0, v75
	v_add_f32_e32 v73, v200, v201
	v_mov_b32_e32 v79, v71
	v_add_f32_e32 v75, v70, v71
	v_pk_add_f32 v[70:71], v[180:181], v[194:195] neg_lo:[0,1] neg_hi:[0,1]
	v_mov_b32_e32 v193, v194
	v_mfma_f32_32x32x16_bf16 v[34:49], v[134:137], v[66:69], v[34:49]
	v_exp_f32_e32 v77, v72
	v_add_f32_e32 v134, 0, v73
	v_pk_add_f32 v[72:73], v[78:79], v[196:197] neg_lo:[0,1] neg_hi:[0,1]
	v_exp_f32_e32 v78, v75
	v_mov_b32_e32 v75, v71
	v_add_f32_e32 v70, v70, v71
	v_add_f32_e32 v71, v72, v73
	v_mfma_f32_32x32x16_bf16 v[50:65], v[168:171], v[66:69], v[50:65]
	v_add_f32_e64 v72, v74, -v192
	v_add_f32_e64 v73, v75, -v193
	v_add_f32_e32 v167, v202, v203
	v_add_f32_e32 v70, 0, v70
	v_exp_f32_e32 v76, v167
	v_exp_f32_e32 v79, v134
	v_exp_f32_e32 v74, v71
	v_exp_f32_e32 v75, v70
	s_waitcnt vmcnt(3)
	v_mfma_f32_32x32x16_bf16 v[18:33], v[176:179], v[66:69], v[18:33]
	v_cvt_pk_bf16_f32 v71, v76, v138
	v_cvt_pk_bf16_f32 v70, v74, v78
	s_waitcnt vmcnt(1)
	v_mfma_f32_32x32x16_bf16 v[2:17], v[130:133], v[66:69], v[2:17]
	v_add_f32_e32 v66, v72, v73
	v_add_f32_e32 v66, 0, v66
	v_exp_f32_e32 v66, v66
	v_cvt_pk_bf16_f32 v69, v79, v77
	v_add_f32_e32 v67, v80, v81
	v_add_f32_e32 v147, v147, v67
	v_cvt_pk_bf16_f32 v68, v66, v75
	v_cmp_gt_f32_e32 vcc, s69, v147
	s_cmp_lg_u64 vcc, exec
	v_mfma_f32_32x32x16_bf16 v[50:65], v[118:121], v[68:71], v[50:65]
	s_cselect_b64 s[42:43], -1, 0
	s_cmp_lg_u32 s64, 0
	s_cselect_b64 s[72:73], -1, 0
	s_and_b64 s[42:43], s[72:73], s[42:43]
	v_mov_b32_e32 v66, s63
	s_add_i32 s64, s64, 1
	s_and_b64 vcc, exec, s[42:43]
	v_mfma_f32_32x32x16_bf16 v[34:49], v[122:125], v[68:71], v[34:49]
	v_mfma_f32_32x32x16_bf16 v[18:33], v[126:129], v[68:71], v[18:33]
	s_waitcnt vmcnt(0)
	v_mfma_f32_32x32x16_bf16 v[2:17], v[114:117], v[68:71], v[2:17]
	s_cbranch_vccnz .LBB0_1664
	s_branch .LBB0_1655

.LBB0_2518:
	s_ashr_i32 s3, s2, 31
	s_lshr_b32 s14, s3, 26
	s_add_i32 s14, s2, s14
	s_ashr_i32 s14, s14, 6
	s_mul_hi_i32 s15, s14, 0xc000
	s_mul_i32 s14, s14, 0xc000
	s_add_u32 s14, s44, s14
	s_addc_u32 s15, s45, s15
	v_lshl_add_u64 v[4:5], v[32:33], 2, s[14:15]
	v_add_co_u32_e32 v4, vcc, s18, v4
	s_waitcnt vmcnt(0)
	s_nop 0
	v_addc_co_u32_e32 v5, vcc, 0, v5, vcc
	s_barrier
	global_load_dwordx4 v[0:3], v[34:35], off
	s_lshl_b64 s[14:15], s[2:3], 7
	global_load_dwordx4 v[4:7], v[4:5], off
	s_add_u32 s16, s14, s9
	s_addc_u32 s17, s15, 0
	s_lshl_b64 s[14:15], s[16:17], 13
	v_lshl_add_u64 v[8:9], v[38:39], 0, s[14:15]
	s_lshl_b64 s[16:17], s[16:17], 12
	v_add_co_u32_e32 v12, vcc, s19, v8
	v_lshl_add_u64 v[10:11], v[40:41], 0, s[16:17]
	s_nop 0
	v_addc_co_u32_e32 v13, vcc, 0, v9, vcc
	s_mov_b64 s[16:17], 0
	v_mov_b64_e32 v[64:65], v[44:45]
	s_waitcnt vmcnt(0)
	v_pk_mul_f32 v[0:1], v[0:1], v[4:5]
	v_pk_mul_f32 v[2:3], v[2:3], v[6:7]
	ds_write_b128 v114, v[0:3]
	s_waitcnt lgkmcnt(0)
	s_barrier
	global_load_dword v145, v[8:9], off
	global_load_dword v141, v[8:9], off offset:256
	global_load_dword v137, v[8:9], off offset:512
	global_load_dword v133, v[8:9], off offset:768
	global_load_dword v129, v[8:9], off offset:1024
	global_load_dword v125, v[8:9], off offset:1280
	global_load_dword v121, v[8:9], off offset:1536
	global_load_dword v117, v[8:9], off offset:1792
	global_load_dword v146, v[8:9], off offset:2048
	global_load_dword v142, v[8:9], off offset:2304
	global_load_dword v138, v[8:9], off offset:2560
	global_load_dword v134, v[8:9], off offset:2816
	global_load_dword v130, v[8:9], off offset:3072
	global_load_dword v126, v[8:9], off offset:3328
	global_load_dword v122, v[8:9], off offset:3584
	global_load_dword v118, v[8:9], off offset:3840
	global_load_dword v147, v[12:13], off
	global_load_dword v143, v[12:13], off offset:256
	global_load_dword v139, v[12:13], off offset:512
	global_load_dword v135, v[12:13], off offset:768
	global_load_dword v131, v[12:13], off offset:1024
	global_load_dword v127, v[12:13], off offset:1280
	global_load_dword v123, v[12:13], off offset:1536
	global_load_dword v119, v[12:13], off offset:1792
	global_load_dword v148, v[12:13], off offset:2048
	global_load_dword v144, v[12:13], off offset:2304
	global_load_dword v140, v[12:13], off offset:2560
	global_load_dword v136, v[12:13], off offset:2816
	global_load_dword v132, v[12:13], off offset:3072
	global_load_dword v128, v[12:13], off offset:3328
	global_load_dword v124, v[12:13], off offset:3584
	global_load_dword v120, v[12:13], off offset:3840
	global_load_dwordx2 v[66:67], v[10:11], off
	global_load_dwordx2 v[60:61], v[10:11], off offset:512
	global_load_dwordx2 v[58:59], v[10:11], off offset:1024
	global_load_dwordx2 v[56:57], v[10:11], off offset:1536
	global_load_dwordx2 v[54:55], v[10:11], off offset:2048
	global_load_dwordx2 v[52:53], v[10:11], off offset:2560
	global_load_dwordx2 v[50:51], v[10:11], off offset:3072
	global_load_dwordx2 v[48:49], v[10:11], off offset:3584
	ds_read_b128 v[28:31], v115
	ds_read_b128 v[24:27], v115 offset:1024
	ds_read_b128 v[20:23], v115 offset:2048
	ds_read_b128 v[16:19], v115 offset:3072
	ds_read_b128 v[12:15], v115 offset:4096
	ds_read_b128 v[8:11], v115 offset:5120
	ds_read_b128 v[4:7], v115 offset:6144
	ds_read_b128 v[0:3], v115 offset:7168
	s_waitcnt vmcnt(0)
.LBB0_2519:
	v_lshl_add_u64 v[158:159], v[46:47], 0, s[16:17]
	v_add_co_u32_e32 v160, vcc, s20, v158
	s_nop 1
	v_addc_co_u32_e32 v161, vcc, 0, v159, vcc
	v_add_co_u32_e32 v158, vcc, s21, v158
	s_nop 1
	v_addc_co_u32_e32 v159, vcc, 0, v159, vcc
	global_load_dword v190, v[158:159], off offset:-4096
	global_load_dword v186, v[160:161], off offset:256
	global_load_dword v182, v[160:161], off offset:512
	global_load_dword v178, v[160:161], off offset:768
	global_load_dword v174, v[160:161], off offset:1024
	global_load_dword v170, v[160:161], off offset:1280
	global_load_dword v166, v[160:161], off offset:1536
	global_load_dword v162, v[160:161], off offset:1792
	global_load_dword v191, v[160:161], off offset:2048
	global_load_dword v187, v[160:161], off offset:2304
	global_load_dword v183, v[160:161], off offset:2560
	global_load_dword v179, v[160:161], off offset:2816
	global_load_dword v175, v[160:161], off offset:3072
	global_load_dword v171, v[160:161], off offset:3328
	global_load_dword v167, v[160:161], off offset:3584
	global_load_dword v163, v[160:161], off offset:3840
	global_load_dword v192, v[158:159], off
	global_load_dword v188, v[158:159], off offset:256
	global_load_dword v184, v[158:159], off offset:512
	global_load_dword v180, v[158:159], off offset:768
	global_load_dword v176, v[158:159], off offset:1024
	global_load_dword v172, v[158:159], off offset:1280
	global_load_dword v168, v[158:159], off offset:1536
	global_load_dword v164, v[158:159], off offset:1792
	global_load_dword v193, v[158:159], off offset:2048
	global_load_dword v189, v[158:159], off offset:2304
	global_load_dword v185, v[158:159], off offset:2560
	global_load_dword v181, v[158:159], off offset:2816
	global_load_dword v177, v[158:159], off offset:3072
	global_load_dword v173, v[158:159], off offset:3328
	global_load_dword v169, v[158:159], off offset:3584
	global_load_dword v165, v[158:159], off offset:3840
	global_load_dwordx2 v[194:195], v[64:65], off offset:-2048
	global_load_dwordx2 v[196:197], v[64:65], off offset:-1536
	global_load_dwordx2 v[198:199], v[64:65], off offset:-1024
	global_load_dwordx2 v[200:201], v[64:65], off offset:-512
	global_load_dwordx2 v[202:203], v[64:65], off
	global_load_dwordx2 v[204:205], v[64:65], off offset:512
	global_load_dwordx2 v[206:207], v[64:65], off offset:1024
	global_load_dwordx2 v[208:209], v[64:65], off offset:1536
	v_mov_b32_e32 v84, v145
	v_mov_b32_e32 v88, v146
	v_cvt_pk_f32_fp8_e32 v[82:83], v84
	v_cvt_pk_f32_fp8_sdwa v[84:85], v84 src0_sel:WORD_1
	v_cvt_pk_f32_fp8_e32 v[86:87], v88
	v_cvt_pk_f32_fp8_sdwa v[88:89], v88 src0_sel:WORD_1
	v_mov_b32_e32 v91, v147
	v_pk_add_f32 v[84:85], v[84:85], 0 op_sel_hi:[1,0]
	v_pk_add_f32 v[82:83], v[82:83], 0 op_sel_hi:[1,0]
	v_pk_add_f32 v[84:85], v[84:85], v[88:89]
	v_pk_add_f32 v[82:83], v[82:83], v[86:87]
	v_cvt_pk_f32_fp8_e32 v[86:87], v91
	v_cvt_pk_f32_fp8_sdwa v[88:89], v91 src0_sel:WORD_1
	v_mov_b32_e32 v93, v148
	v_mov_b32_e32 v90, v141
	v_pk_add_f32 v[82:83], v[82:83], v[86:87]
	v_pk_add_f32 v[84:85], v[84:85], v[88:89]
	v_cvt_pk_f32_fp8_e32 v[86:87], v93
	v_cvt_pk_f32_fp8_sdwa v[88:89], v93 src0_sel:WORD_1
	v_mov_b32_e32 v92, v142
	v_mov_b32_e32 v95, v143
	v_pk_add_f32 v[86:87], v[82:83], v[86:87]
	v_pk_add_f32 v[82:83], v[84:85], v[88:89]
	v_cvt_pk_f32_fp8_e32 v[84:85], v90
	v_cvt_pk_f32_fp8_sdwa v[88:89], v90 src0_sel:WORD_1
	v_cvt_pk_f32_fp8_e32 v[90:91], v92
	v_cvt_pk_f32_fp8_sdwa v[92:93], v92 src0_sel:WORD_1
	v_pk_add_f32 v[84:85], v[84:85], 0 op_sel_hi:[1,0]
	v_pk_add_f32 v[88:89], v[88:89], 0 op_sel_hi:[1,0]
	v_pk_add_f32 v[84:85], v[84:85], v[90:91]
	v_cvt_pk_f32_fp8_e32 v[90:91], v95
	v_pk_add_f32 v[88:89], v[88:89], v[92:93]
	v_cvt_pk_f32_fp8_sdwa v[92:93], v95 src0_sel:WORD_1
	v_mov_b32_e32 v97, v144
	v_pk_add_f32 v[84:85], v[84:85], v[90:91]
	v_cvt_pk_f32_fp8_e32 v[90:91], v97
	v_pk_add_f32 v[88:89], v[88:89], v[92:93]
	v_cvt_pk_f32_fp8_sdwa v[92:93], v97 src0_sel:WORD_1
	v_pk_mul_f32 v[86:87], v[86:87], s[8:9] op_sel_hi:[1,0]
	v_pk_add_f32 v[90:91], v[84:85], v[90:91]
	v_mul_f32_e32 v153, v87, v87
	v_pk_add_f32 v[84:85], v[88:89], v[92:93]
	v_pk_mul_f32 v[88:89], v[90:91], s[8:9] op_sel_hi:[1,0]
	v_pk_mul_f32 v[82:83], v[82:83], s[8:9] op_sel_hi:[1,0]
	v_mul_f32_e32 v90, v89, v89
	v_fmac_f32_e32 v153, v86, v86
	v_pk_mul_f32 v[84:85], v[84:85], s[8:9] op_sel_hi:[1,0]
	v_fmac_f32_e32 v90, v88, v88
	v_fmac_f32_e32 v153, v82, v82
	v_fmac_f32_e32 v90, v84, v84
	v_mov_b32_e32 v94, v137
	v_fmac_f32_e32 v153, v83, v83
	v_fmac_f32_e32 v90, v85, v85
	v_mov_b32_e32 v96, v138
	v_add_f32_e32 v153, v153, v90
	v_cvt_pk_f32_fp8_e32 v[90:91], v94
	v_cvt_pk_f32_fp8_sdwa v[92:93], v94 src0_sel:WORD_1
	v_cvt_pk_f32_fp8_e32 v[94:95], v96
	v_cvt_pk_f32_fp8_sdwa v[96:97], v96 src0_sel:WORD_1
	v_mov_b32_e32 v99, v139
	v_pk_add_f32 v[90:91], v[90:91], 0 op_sel_hi:[1,0]
	v_pk_add_f32 v[92:93], v[92:93], 0 op_sel_hi:[1,0]
	v_pk_add_f32 v[90:91], v[90:91], v[94:95]
	v_cvt_pk_f32_fp8_e32 v[94:95], v99
	v_pk_add_f32 v[92:93], v[92:93], v[96:97]
	v_cvt_pk_f32_fp8_sdwa v[96:97], v99 src0_sel:WORD_1
	v_mov_b32_e32 v101, v140
	v_pk_add_f32 v[90:91], v[90:91], v[94:95]
	v_cvt_pk_f32_fp8_e32 v[94:95], v101
	v_pk_add_f32 v[92:93], v[92:93], v[96:97]
	v_cvt_pk_f32_fp8_sdwa v[96:97], v101 src0_sel:WORD_1
	v_mov_b32_e32 v98, v133
	v_pk_add_f32 v[94:95], v[90:91], v[94:95]
	v_mov_b32_e32 v100, v134
	v_pk_add_f32 v[90:91], v[92:93], v[96:97]
	v_pk_mul_f32 v[92:93], v[94:95], s[8:9] op_sel_hi:[1,0]
	v_pk_mul_f32 v[90:91], v[90:91], s[8:9] op_sel_hi:[1,0]
	v_mul_f32_e32 v94, v93, v93
	v_fmac_f32_e32 v94, v92, v92
	v_fmac_f32_e32 v94, v90, v90
	v_fmac_f32_e32 v94, v91, v91
	v_add_f32_e32 v153, v153, v94
	v_cvt_pk_f32_fp8_e32 v[94:95], v98
	v_cvt_pk_f32_fp8_sdwa v[96:97], v98 src0_sel:WORD_1
	v_cvt_pk_f32_fp8_e32 v[98:99], v100
	v_cvt_pk_f32_fp8_sdwa v[100:101], v100 src0_sel:WORD_1
	v_mov_b32_e32 v103, v135
	v_pk_add_f32 v[94:95], v[94:95], 0 op_sel_hi:[1,0]
	v_pk_add_f32 v[96:97], v[96:97], 0 op_sel_hi:[1,0]
	v_pk_add_f32 v[94:95], v[94:95], v[98:99]
	v_cvt_pk_f32_fp8_e32 v[98:99], v103
	v_pk_add_f32 v[96:97], v[96:97], v[100:101]
	v_cvt_pk_f32_fp8_sdwa v[100:101], v103 src0_sel:WORD_1
	v_mov_b32_e32 v105, v136
	v_pk_add_f32 v[94:95], v[94:95], v[98:99]
	v_cvt_pk_f32_fp8_e32 v[98:99], v105
	v_pk_add_f32 v[96:97], v[96:97], v[100:101]
	v_cvt_pk_f32_fp8_sdwa v[100:101], v105 src0_sel:WORD_1
	v_mov_b32_e32 v102, v129
	v_pk_add_f32 v[98:99], v[94:95], v[98:99]
	v_mov_b32_e32 v104, v130
	v_pk_add_f32 v[94:95], v[96:97], v[100:101]
	v_pk_mul_f32 v[96:97], v[98:99], s[8:9] op_sel_hi:[1,0]
	v_pk_mul_f32 v[94:95], v[94:95], s[8:9] op_sel_hi:[1,0]
	v_mul_f32_e32 v98, v97, v97
	v_fmac_f32_e32 v98, v96, v96
	v_fmac_f32_e32 v98, v94, v94
	v_fmac_f32_e32 v98, v95, v95
	v_add_f32_e32 v153, v153, v98
	v_cvt_pk_f32_fp8_e32 v[98:99], v102
	v_cvt_pk_f32_fp8_sdwa v[100:101], v102 src0_sel:WORD_1
	v_cvt_pk_f32_fp8_e32 v[102:103], v104
	v_cvt_pk_f32_fp8_sdwa v[104:105], v104 src0_sel:WORD_1
	v_mov_b32_e32 v107, v131
	v_pk_add_f32 v[98:99], v[98:99], 0 op_sel_hi:[1,0]
	v_pk_add_f32 v[100:101], v[100:101], 0 op_sel_hi:[1,0]
	v_pk_add_f32 v[98:99], v[98:99], v[102:103]
	v_cvt_pk_f32_fp8_e32 v[102:103], v107
	v_pk_add_f32 v[100:101], v[100:101], v[104:105]
	v_cvt_pk_f32_fp8_sdwa v[104:105], v107 src0_sel:WORD_1
	v_mov_b32_e32 v109, v132
	v_pk_add_f32 v[98:99], v[98:99], v[102:103]
	v_cvt_pk_f32_fp8_e32 v[102:103], v109
	v_pk_add_f32 v[100:101], v[100:101], v[104:105]
	v_cvt_pk_f32_fp8_sdwa v[104:105], v109 src0_sel:WORD_1
	v_mov_b32_e32 v106, v125
	v_pk_add_f32 v[102:103], v[98:99], v[102:103]
	v_mov_b32_e32 v108, v126
	v_pk_add_f32 v[98:99], v[100:101], v[104:105]
	v_pk_mul_f32 v[100:101], v[102:103], s[8:9] op_sel_hi:[1,0]
	v_pk_mul_f32 v[98:99], v[98:99], s[8:9] op_sel_hi:[1,0]
	v_mul_f32_e32 v102, v101, v101
	v_fmac_f32_e32 v102, v100, v100
	v_fmac_f32_e32 v102, v98, v98
	v_fmac_f32_e32 v102, v99, v99
	v_add_f32_e32 v153, v153, v102
	v_cvt_pk_f32_fp8_e32 v[102:103], v106
	v_cvt_pk_f32_fp8_sdwa v[104:105], v106 src0_sel:WORD_1
	v_cvt_pk_f32_fp8_e32 v[106:107], v108
	v_cvt_pk_f32_fp8_sdwa v[108:109], v108 src0_sel:WORD_1
	v_mov_b32_e32 v111, v127
	v_pk_add_f32 v[102:103], v[102:103], 0 op_sel_hi:[1,0]
	v_pk_add_f32 v[104:105], v[104:105], 0 op_sel_hi:[1,0]
	v_pk_add_f32 v[102:103], v[102:103], v[106:107]
	v_cvt_pk_f32_fp8_e32 v[106:107], v111
	v_pk_add_f32 v[104:105], v[104:105], v[108:109]
	v_cvt_pk_f32_fp8_sdwa v[108:109], v111 src0_sel:WORD_1
	v_mov_b32_e32 v113, v128
	v_pk_add_f32 v[102:103], v[102:103], v[106:107]
	v_cvt_pk_f32_fp8_e32 v[106:107], v113
	v_pk_add_f32 v[104:105], v[104:105], v[108:109]
	v_cvt_pk_f32_fp8_sdwa v[108:109], v113 src0_sel:WORD_1
	v_mov_b64_e32 v[68:69], v[48:49]
	v_pk_add_f32 v[106:107], v[102:103], v[106:107]
	v_pk_add_f32 v[102:103], v[104:105], v[108:109]
	v_pk_mul_f32 v[104:105], v[106:107], s[8:9] op_sel_hi:[1,0]
	v_mov_b64_e32 v[70:71], v[50:51]
	v_mul_f32_e32 v106, v105, v105
	v_pk_mul_f32 v[102:103], v[102:103], s[8:9] op_sel_hi:[1,0]
	v_fmac_f32_e32 v106, v104, v104
	v_fmac_f32_e32 v106, v102, v102
	v_mov_b32_e32 v110, v121
	v_fmac_f32_e32 v106, v103, v103
	v_mov_b32_e32 v112, v122
	v_add_f32_e32 v153, v153, v106
	v_cvt_pk_f32_fp8_e32 v[106:107], v110
	v_mov_b64_e32 v[80:81], v[60:61]
	v_mov_b64_e32 v[78:79], v[58:59]
	v_mov_b64_e32 v[76:77], v[56:57]
	v_mov_b64_e32 v[74:75], v[54:55]
	v_mov_b64_e32 v[72:73], v[52:53]
	v_mov_b32_e32 v149, v117
	v_mov_b32_e32 v152, v118
	v_mov_b32_e32 v150, v123
	v_mov_b32_e32 v154, v119
	v_mov_b32_e32 v151, v124
	v_mov_b32_e32 v155, v120
	v_cvt_pk_f32_fp8_sdwa v[108:109], v110 src0_sel:WORD_1
	v_cvt_pk_f32_fp8_e32 v[110:111], v112
	v_cvt_pk_f32_fp8_sdwa v[112:113], v112 src0_sel:WORD_1
	v_pk_add_f32 v[106:107], v[106:107], 0 op_sel_hi:[1,0]
	v_pk_add_f32 v[108:109], v[108:109], 0 op_sel_hi:[1,0]
	v_pk_add_f32 v[106:107], v[106:107], v[110:111]
	v_cvt_pk_f32_fp8_e32 v[110:111], v150
	v_pk_add_f32 v[108:109], v[108:109], v[112:113]
	v_cvt_pk_f32_fp8_sdwa v[112:113], v150 src0_sel:WORD_1
	v_lshl_add_u64 v[64:65], v[64:65], 0, s[10:11]
	v_pk_add_f32 v[106:107], v[106:107], v[110:111]
	v_cvt_pk_f32_fp8_e32 v[110:111], v151
	v_pk_add_f32 v[108:109], v[108:109], v[112:113]
	v_cvt_pk_f32_fp8_sdwa v[112:113], v151 src0_sel:WORD_1
	v_cvt_pk_f32_fp8_e32 v[150:151], v152
	v_pk_add_f32 v[110:111], v[106:107], v[110:111]
	v_pk_add_f32 v[106:107], v[108:109], v[112:113]
	v_pk_mul_f32 v[108:109], v[110:111], s[8:9] op_sel_hi:[1,0]
	v_pk_mul_f32 v[106:107], v[106:107], s[8:9] op_sel_hi:[1,0]
	v_mul_f32_e32 v110, v109, v109
	v_fmac_f32_e32 v110, v108, v108
	v_fmac_f32_e32 v110, v106, v106
	v_fmac_f32_e32 v110, v107, v107
	v_add_f32_e32 v156, v153, v110
	v_cvt_pk_f32_fp8_e32 v[110:111], v149
	v_cvt_pk_f32_fp8_sdwa v[112:113], v149 src0_sel:WORD_1
	v_cvt_pk_f32_fp8_sdwa v[152:153], v152 src0_sel:WORD_1
	v_pk_add_f32 v[110:111], v[110:111], 0 op_sel_hi:[1,0]
	v_pk_add_f32 v[112:113], v[112:113], 0 op_sel_hi:[1,0]
	v_pk_add_f32 v[110:111], v[110:111], v[150:151]
	v_cvt_pk_f32_fp8_e32 v[150:151], v154
	v_pk_add_f32 v[112:113], v[112:113], v[152:153]
	v_cvt_pk_f32_fp8_sdwa v[152:153], v154 src0_sel:WORD_1
	v_pk_add_f32 v[110:111], v[110:111], v[150:151]
	v_cvt_pk_f32_fp8_e32 v[150:151], v155
	v_pk_add_f32 v[112:113], v[112:113], v[152:153]
	v_cvt_pk_f32_fp8_sdwa v[152:153], v155 src0_sel:WORD_1
	v_lshl_add_u64 v[154:155], v[42:43], 0, s[16:17]
	v_pk_add_f32 v[150:151], v[110:111], v[150:151]
	s_add_u32 s16, s16, 0x2000
	v_pk_add_f32 v[110:111], v[112:113], v[152:153]
	v_pk_mul_f32 v[112:113], v[150:151], s[8:9] op_sel_hi:[1,0]
	v_pk_mul_f32 v[110:111], v[110:111], s[8:9] op_sel_hi:[1,0]
	v_mul_f32_e32 v149, v113, v113
	v_fmac_f32_e32 v149, v112, v112
	v_fmac_f32_e32 v149, v110, v110
	v_fmac_f32_e32 v149, v111, v111
	v_add_f32_e32 v149, v156, v149
	v_and_b32_e32 v151, 0xffff0000, v66
	s_addc_u32 s17, s17, 0
	v_add_f32_dpp v149, v149, v149 quad_perm:[1,0,3,2] row_mask:0xf bank_mask:0xf bound_ctrl:1
	s_cmp_eq_u32 s16, 0x1e000
	s_nop 0
	v_add_f32_dpp v149, v149, v149 quad_perm:[2,3,0,1] row_mask:0xf bank_mask:0xf bound_ctrl:1
	s_nop 1
	v_add_f32_dpp v149, v149, v149 row_half_mirror row_mask:0xf bank_mask:0xf bound_ctrl:1
	s_nop 1
	v_add_f32_dpp v149, v149, v149 row_mirror row_mask:0xf bank_mask:0xf bound_ctrl:1
	v_mov_b32_e32 v150, v149
	s_nop 1
	v_permlane16_swap_b32_e32 v149, v150
	v_add_f32_e32 v149, v149, v150
	v_mov_b32_e32 v150, v149
	s_nop 1
	v_permlane32_swap_b32_e32 v149, v150
	v_add_f32_e32 v149, v149, v150
	v_fmamk_f32 v149, v149, 0x3a000000, v116
	v_cmp_gt_f32_e32 vcc, s22, v149
	v_mul_f32_e32 v150, 0x4b800000, v149
	s_nop 0
	v_cndmask_b32_e32 v149, v149, v150, vcc
	v_rsq_f32_e32 v149, v149
	s_nop 0
	v_mul_f32_e32 v150, 0x45800000, v149
	v_cndmask_b32_e32 v156, v149, v150, vcc
	v_lshlrev_b32_e32 v150, 16, v66
	v_lshlrev_b32_e32 v66, 16, v67
	v_and_b32_e32 v67, 0xffff0000, v67
	v_pk_mul_f32 v[82:83], v[82:83], v[156:157] op_sel_hi:[1,0]
	v_pk_mul_f32 v[86:87], v[86:87], v[156:157] op_sel_hi:[1,0]
	s_waitcnt lgkmcnt(7)
	v_pk_fma_f32 v[152:153], v[30:31], v[82:83], v[66:67]
	v_lshlrev_b32_e32 v66, 16, v80
	v_and_b32_e32 v67, 0xffff0000, v80
	v_pk_mul_f32 v[82:83], v[88:89], v[156:157] op_sel_hi:[1,0]
	v_pk_fma_f32 v[150:151], v[28:29], v[86:87], v[150:151]
	s_waitcnt lgkmcnt(6)
	v_pk_fma_f32 v[82:83], v[24:25], v[82:83], v[66:67]
	v_lshlrev_b32_e32 v66, 16, v81
	v_and_b32_e32 v67, 0xffff0000, v81
	v_pk_mul_f32 v[80:81], v[84:85], v[156:157] op_sel_hi:[1,0]
	global_store_dwordx4 v[154:155], v[150:153], off nt
	v_pk_fma_f32 v[84:85], v[26:27], v[80:81], v[66:67]
	v_lshlrev_b32_e32 v66, 16, v78
	v_and_b32_e32 v67, 0xffff0000, v78
	v_pk_mul_f32 v[80:81], v[92:93], v[156:157] op_sel_hi:[1,0]
	global_store_dwordx4 v[154:155], v[82:85], off offset:1024 nt
	s_waitcnt lgkmcnt(5)
	v_pk_fma_f32 v[80:81], v[80:81], v[20:21], v[66:67]
	v_lshlrev_b32_e32 v66, 16, v79
	v_and_b32_e32 v67, 0xffff0000, v79
	v_pk_mul_f32 v[78:79], v[90:91], v[156:157] op_sel_hi:[1,0]
	s_nop 0
	v_pk_fma_f32 v[82:83], v[78:79], v[22:23], v[66:67]
	v_lshlrev_b32_e32 v66, 16, v76
	v_and_b32_e32 v67, 0xffff0000, v76
	v_pk_mul_f32 v[78:79], v[96:97], v[156:157] op_sel_hi:[1,0]
	global_store_dwordx4 v[154:155], v[80:83], off offset:2048 nt
	s_waitcnt lgkmcnt(4)
	v_pk_fma_f32 v[78:79], v[78:79], v[16:17], v[66:67]
	v_lshlrev_b32_e32 v66, 16, v77
	v_and_b32_e32 v67, 0xffff0000, v77
	v_pk_mul_f32 v[76:77], v[94:95], v[156:157] op_sel_hi:[1,0]
	s_nop 0
	v_pk_fma_f32 v[80:81], v[76:77], v[18:19], v[66:67]
	v_lshlrev_b32_e32 v66, 16, v74
	v_and_b32_e32 v67, 0xffff0000, v74
	v_pk_mul_f32 v[76:77], v[100:101], v[156:157] op_sel_hi:[1,0]
	global_store_dwordx4 v[154:155], v[78:81], off offset:3072 nt
	s_waitcnt lgkmcnt(3)
	v_pk_fma_f32 v[76:77], v[76:77], v[12:13], v[66:67]
	v_lshlrev_b32_e32 v66, 16, v75
	v_and_b32_e32 v67, 0xffff0000, v75
	v_pk_mul_f32 v[74:75], v[98:99], v[156:157] op_sel_hi:[1,0]
	v_add_co_u32_e32 v80, vcc, s19, v154
	v_pk_fma_f32 v[78:79], v[74:75], v[14:15], v[66:67]
	v_lshlrev_b32_e32 v66, 16, v72
	v_and_b32_e32 v67, 0xffff0000, v72
	v_pk_mul_f32 v[74:75], v[104:105], v[156:157] op_sel_hi:[1,0]
	v_addc_co_u32_e32 v81, vcc, 0, v155, vcc
	s_waitcnt lgkmcnt(2)
	v_pk_fma_f32 v[74:75], v[74:75], v[8:9], v[66:67]
	v_lshlrev_b32_e32 v66, 16, v73
	v_and_b32_e32 v67, 0xffff0000, v73
	v_pk_mul_f32 v[72:73], v[102:103], v[156:157] op_sel_hi:[1,0]
	global_store_dwordx4 v[80:81], v[76:79], off nt
	s_nop 1
	v_pk_fma_f32 v[76:77], v[72:73], v[10:11], v[66:67]
	v_lshlrev_b32_e32 v66, 16, v70
	v_and_b32_e32 v67, 0xffff0000, v70
	v_pk_mul_f32 v[72:73], v[108:109], v[156:157] op_sel_hi:[1,0]
	global_store_dwordx4 v[80:81], v[74:77], off offset:1024 nt
	s_waitcnt lgkmcnt(1)
	v_pk_fma_f32 v[72:73], v[72:73], v[4:5], v[66:67]
	v_lshlrev_b32_e32 v66, 16, v71
	v_and_b32_e32 v67, 0xffff0000, v71
	v_pk_mul_f32 v[70:71], v[106:107], v[156:157] op_sel_hi:[1,0]
	s_nop 0
	v_pk_fma_f32 v[74:75], v[70:71], v[6:7], v[66:67]
	v_lshlrev_b32_e32 v66, 16, v68
	v_and_b32_e32 v67, 0xffff0000, v68
	v_pk_mul_f32 v[70:71], v[112:113], v[156:157] op_sel_hi:[1,0]
	v_lshlrev_b32_e32 v68, 16, v69
	s_waitcnt lgkmcnt(0)
	v_pk_fma_f32 v[66:67], v[70:71], v[0:1], v[66:67]
	v_and_b32_e32 v69, 0xffff0000, v69
	v_pk_mul_f32 v[70:71], v[110:111], v[156:157] op_sel_hi:[1,0]
	global_store_dwordx4 v[80:81], v[72:75], off offset:2048 nt
	v_pk_fma_f32 v[68:69], v[70:71], v[2:3], v[68:69]
	global_store_dwordx4 v[80:81], v[66:69], off offset:3072 nt
	s_waitcnt vmcnt(8)
	s_nop 0
	v_mov_b32_e32 v145, v190
	v_mov_b32_e32 v141, v186
	v_mov_b32_e32 v137, v182
	v_mov_b32_e32 v133, v178
	v_mov_b32_e32 v129, v174
	v_mov_b32_e32 v125, v170
	v_mov_b32_e32 v121, v166
	v_mov_b32_e32 v117, v162
	v_mov_b32_e32 v146, v191
	v_mov_b32_e32 v142, v187
	v_mov_b32_e32 v138, v183
	v_mov_b32_e32 v134, v179
	v_mov_b32_e32 v130, v175
	v_mov_b32_e32 v126, v171
	v_mov_b32_e32 v122, v167
	v_mov_b32_e32 v118, v163
	v_mov_b32_e32 v147, v192
	v_mov_b32_e32 v143, v188
	v_mov_b32_e32 v139, v184
	v_mov_b32_e32 v135, v180
	v_mov_b32_e32 v131, v176
	v_mov_b32_e32 v127, v172
	v_mov_b32_e32 v123, v168
	v_mov_b32_e32 v119, v164
	v_mov_b32_e32 v148, v193
	v_mov_b32_e32 v144, v189
	v_mov_b32_e32 v140, v185
	v_mov_b32_e32 v136, v181
	v_mov_b32_e32 v132, v177
	v_mov_b32_e32 v128, v173
	v_mov_b32_e32 v124, v169
	v_mov_b32_e32 v120, v165
	v_mov_b64_e32 v[66:67], v[194:195]
	v_mov_b64_e32 v[62:63], v[194:195]
	v_mov_b64_e32 v[60:61], v[196:197]
	v_mov_b64_e32 v[58:59], v[198:199]
	v_mov_b64_e32 v[56:57], v[200:201]
	v_mov_b64_e32 v[54:55], v[202:203]
	v_mov_b64_e32 v[52:53], v[204:205]
	v_mov_b64_e32 v[50:51], v[206:207]
	v_mov_b64_e32 v[48:49], v[208:209]
	s_cbranch_scc0 .LBB0_2519
	v_cvt_pk_f32_fp8_e32 v[66:67], v145
	v_cvt_pk_f32_fp8_e32 v[68:69], v146
	v_cvt_pk_f32_fp8_sdwa v[64:65], v145 src0_sel:WORD_1
	v_cvt_pk_f32_fp8_sdwa v[70:71], v146 src0_sel:WORD_1
	v_pk_add_f32 v[66:67], v[66:67], 0 op_sel_hi:[1,0]
	v_cvt_pk_f32_fp8_sdwa v[74:75], v148 src0_sel:WORD_1
	v_pk_add_f32 v[66:67], v[66:67], v[68:69]
	v_cvt_pk_f32_fp8_sdwa v[68:69], v147 src0_sel:WORD_1
	v_pk_add_f32 v[64:65], v[64:65], 0 op_sel_hi:[1,0]
	v_cvt_pk_f32_fp8_e32 v[72:73], v148
	v_pk_add_f32 v[64:65], v[64:65], v[70:71]
	v_cvt_pk_f32_fp8_e32 v[70:71], v147
	v_pk_add_f32 v[64:65], v[64:65], v[68:69]
	v_cvt_pk_f32_fp8_sdwa v[68:69], v141 src0_sel:WORD_1
	v_pk_add_f32 v[64:65], v[64:65], v[74:75]
	v_cvt_pk_f32_fp8_sdwa v[74:75], v142 src0_sel:WORD_1
	v_pk_add_f32 v[66:67], v[66:67], v[70:71]
	v_cvt_pk_f32_fp8_e32 v[70:71], v141
	v_pk_add_f32 v[66:67], v[66:67], v[72:73]
	v_cvt_pk_f32_fp8_e32 v[72:73], v142
	v_pk_add_f32 v[68:69], v[68:69], 0 op_sel_hi:[1,0]
	v_pk_add_f32 v[70:71], v[70:71], 0 op_sel_hi:[1,0]
	v_pk_add_f32 v[68:69], v[68:69], v[74:75]
	v_cvt_pk_f32_fp8_e32 v[74:75], v143
	v_cvt_pk_f32_fp8_e32 v[76:77], v144
	v_pk_add_f32 v[70:71], v[70:71], v[72:73]
	v_cvt_pk_f32_fp8_sdwa v[72:73], v143 src0_sel:WORD_1
	v_cvt_pk_f32_fp8_sdwa v[78:79], v144 src0_sel:WORD_1
	v_pk_add_f32 v[70:71], v[70:71], v[74:75]
	v_pk_mul_f32 v[66:67], v[66:67], s[8:9] op_sel_hi:[1,0]
	v_pk_add_f32 v[70:71], v[70:71], v[76:77]
	v_pk_add_f32 v[68:69], v[68:69], v[72:73]
	v_pk_mul_f32 v[70:71], v[70:71], s[8:9] op_sel_hi:[1,0]
	v_mul_f32_e32 v80, v67, v67
	v_pk_add_f32 v[68:69], v[68:69], v[78:79]
	v_mul_f32_e32 v72, v71, v71
	v_pk_mul_f32 v[64:65], v[64:65], s[8:9] op_sel_hi:[1,0]
	v_fmac_f32_e32 v80, v66, v66
	v_pk_mul_f32 v[68:69], v[68:69], s[8:9] op_sel_hi:[1,0]
	v_fmac_f32_e32 v72, v70, v70
	v_fmac_f32_e32 v80, v64, v64
	v_fmac_f32_e32 v72, v68, v68
	v_fmac_f32_e32 v80, v65, v65
	v_fmac_f32_e32 v72, v69, v69
	v_add_f32_e32 v84, v80, v72
	v_cvt_pk_f32_fp8_sdwa v[72:73], v137 src0_sel:WORD_1
	v_cvt_pk_f32_fp8_sdwa v[78:79], v138 src0_sel:WORD_1
	v_cvt_pk_f32_fp8_e32 v[74:75], v137
	v_cvt_pk_f32_fp8_e32 v[76:77], v138
	v_pk_add_f32 v[72:73], v[72:73], 0 op_sel_hi:[1,0]
	v_cvt_pk_f32_fp8_e32 v[80:81], v140
	v_pk_add_f32 v[72:73], v[72:73], v[78:79]
	v_cvt_pk_f32_fp8_e32 v[78:79], v139
	v_pk_add_f32 v[74:75], v[74:75], 0 op_sel_hi:[1,0]
	v_cvt_pk_f32_fp8_sdwa v[82:83], v140 src0_sel:WORD_1
	v_pk_add_f32 v[74:75], v[74:75], v[76:77]
	v_cvt_pk_f32_fp8_sdwa v[76:77], v139 src0_sel:WORD_1
	v_pk_add_f32 v[74:75], v[74:75], v[78:79]
	v_cvt_pk_f32_fp8_e32 v[78:79], v133
	v_pk_add_f32 v[74:75], v[74:75], v[80:81]
	v_pk_add_f32 v[72:73], v[72:73], v[76:77]
	v_pk_mul_f32 v[74:75], v[74:75], s[8:9] op_sel_hi:[1,0]
	v_pk_add_f32 v[72:73], v[72:73], v[82:83]
	v_mul_f32_e32 v76, v75, v75
	v_pk_mul_f32 v[72:73], v[72:73], s[8:9] op_sel_hi:[1,0]
	v_fmac_f32_e32 v76, v74, v74
	v_fmac_f32_e32 v76, v72, v72
	v_fmac_f32_e32 v76, v73, v73
	v_add_f32_e32 v88, v84, v76
	v_cvt_pk_f32_fp8_sdwa v[76:77], v133 src0_sel:WORD_1
	v_cvt_pk_f32_fp8_sdwa v[82:83], v134 src0_sel:WORD_1
	v_cvt_pk_f32_fp8_e32 v[80:81], v134
	v_pk_add_f32 v[78:79], v[78:79], 0 op_sel_hi:[1,0]
	v_pk_add_f32 v[76:77], v[76:77], 0 op_sel_hi:[1,0]
	v_cvt_pk_f32_fp8_e32 v[84:85], v136
	v_pk_add_f32 v[76:77], v[76:77], v[82:83]
	v_cvt_pk_f32_fp8_e32 v[82:83], v135
	v_pk_add_f32 v[78:79], v[78:79], v[80:81]
	v_cvt_pk_f32_fp8_sdwa v[80:81], v135 src0_sel:WORD_1
	v_cvt_pk_f32_fp8_sdwa v[86:87], v136 src0_sel:WORD_1
	v_pk_add_f32 v[78:79], v[78:79], v[82:83]
	v_cvt_pk_f32_fp8_e32 v[82:83], v129
	v_pk_add_f32 v[78:79], v[78:79], v[84:85]
	v_pk_add_f32 v[76:77], v[76:77], v[80:81]
	v_pk_mul_f32 v[78:79], v[78:79], s[8:9] op_sel_hi:[1,0]
	v_pk_add_f32 v[76:77], v[76:77], v[86:87]
	v_mul_f32_e32 v80, v79, v79
	v_pk_mul_f32 v[76:77], v[76:77], s[8:9] op_sel_hi:[1,0]
	v_fmac_f32_e32 v80, v78, v78
	v_fmac_f32_e32 v80, v76, v76
	v_fmac_f32_e32 v80, v77, v77
	v_add_f32_e32 v92, v88, v80
	v_cvt_pk_f32_fp8_sdwa v[80:81], v129 src0_sel:WORD_1
	v_cvt_pk_f32_fp8_sdwa v[86:87], v130 src0_sel:WORD_1
	v_cvt_pk_f32_fp8_e32 v[84:85], v130
	v_pk_add_f32 v[82:83], v[82:83], 0 op_sel_hi:[1,0]
	v_pk_add_f32 v[80:81], v[80:81], 0 op_sel_hi:[1,0]
	v_cvt_pk_f32_fp8_e32 v[88:89], v132
	v_pk_add_f32 v[80:81], v[80:81], v[86:87]
	v_cvt_pk_f32_fp8_e32 v[86:87], v131
	v_pk_add_f32 v[82:83], v[82:83], v[84:85]
	v_cvt_pk_f32_fp8_sdwa v[84:85], v131 src0_sel:WORD_1
	v_cvt_pk_f32_fp8_sdwa v[90:91], v132 src0_sel:WORD_1
	v_pk_add_f32 v[82:83], v[82:83], v[86:87]
	v_cvt_pk_f32_fp8_e32 v[86:87], v125
	v_pk_add_f32 v[82:83], v[82:83], v[88:89]
	v_pk_add_f32 v[80:81], v[80:81], v[84:85]
	v_pk_mul_f32 v[82:83], v[82:83], s[8:9] op_sel_hi:[1,0]
	v_pk_add_f32 v[80:81], v[80:81], v[90:91]
	v_mul_f32_e32 v84, v83, v83
	v_pk_mul_f32 v[80:81], v[80:81], s[8:9] op_sel_hi:[1,0]
	v_fmac_f32_e32 v84, v82, v82
	v_fmac_f32_e32 v84, v80, v80
	v_fmac_f32_e32 v84, v81, v81
	v_add_f32_e32 v96, v92, v84
	v_cvt_pk_f32_fp8_sdwa v[84:85], v125 src0_sel:WORD_1
	v_cvt_pk_f32_fp8_sdwa v[90:91], v126 src0_sel:WORD_1
	v_cvt_pk_f32_fp8_e32 v[88:89], v126
	v_pk_add_f32 v[86:87], v[86:87], 0 op_sel_hi:[1,0]
	v_pk_add_f32 v[84:85], v[84:85], 0 op_sel_hi:[1,0]
	v_cvt_pk_f32_fp8_e32 v[92:93], v128
	v_pk_add_f32 v[84:85], v[84:85], v[90:91]
	v_cvt_pk_f32_fp8_e32 v[90:91], v127
	v_pk_add_f32 v[86:87], v[86:87], v[88:89]
	v_cvt_pk_f32_fp8_sdwa v[88:89], v127 src0_sel:WORD_1
	v_cvt_pk_f32_fp8_sdwa v[94:95], v128 src0_sel:WORD_1
	v_pk_add_f32 v[86:87], v[86:87], v[90:91]
	v_cvt_pk_f32_fp8_e32 v[90:91], v121
	v_pk_add_f32 v[86:87], v[86:87], v[92:93]
	v_pk_add_f32 v[84:85], v[84:85], v[88:89]
	v_pk_mul_f32 v[86:87], v[86:87], s[8:9] op_sel_hi:[1,0]
	v_pk_add_f32 v[84:85], v[84:85], v[94:95]
	v_mul_f32_e32 v88, v87, v87
	v_pk_mul_f32 v[84:85], v[84:85], s[8:9] op_sel_hi:[1,0]
	v_fmac_f32_e32 v88, v86, v86
	v_fmac_f32_e32 v88, v84, v84
	v_fmac_f32_e32 v88, v85, v85
	v_add_f32_e32 v100, v96, v88
	v_cvt_pk_f32_fp8_sdwa v[88:89], v121 src0_sel:WORD_1
	v_cvt_pk_f32_fp8_sdwa v[94:95], v122 src0_sel:WORD_1
	v_cvt_pk_f32_fp8_e32 v[92:93], v122
	v_pk_add_f32 v[90:91], v[90:91], 0 op_sel_hi:[1,0]
	v_pk_add_f32 v[88:89], v[88:89], 0 op_sel_hi:[1,0]
	v_cvt_pk_f32_fp8_e32 v[96:97], v124
	v_pk_add_f32 v[88:89], v[88:89], v[94:95]
	v_cvt_pk_f32_fp8_e32 v[94:95], v123
	v_pk_add_f32 v[90:91], v[90:91], v[92:93]
	v_cvt_pk_f32_fp8_sdwa v[92:93], v123 src0_sel:WORD_1
	v_cvt_pk_f32_fp8_sdwa v[98:99], v124 src0_sel:WORD_1
	v_pk_add_f32 v[90:91], v[90:91], v[94:95]
	v_cvt_pk_f32_fp8_e32 v[94:95], v117
	v_pk_add_f32 v[90:91], v[90:91], v[96:97]
	v_pk_add_f32 v[88:89], v[88:89], v[92:93]
	v_pk_mul_f32 v[90:91], v[90:91], s[8:9] op_sel_hi:[1,0]
	v_pk_add_f32 v[88:89], v[88:89], v[98:99]
	v_mul_f32_e32 v92, v91, v91
	v_pk_mul_f32 v[88:89], v[88:89], s[8:9] op_sel_hi:[1,0]
	v_fmac_f32_e32 v92, v90, v90
	v_fmac_f32_e32 v92, v88, v88
	v_fmac_f32_e32 v92, v89, v89
	v_add_f32_e32 v104, v100, v92
	v_cvt_pk_f32_fp8_sdwa v[92:93], v117 src0_sel:WORD_1
	v_cvt_pk_f32_fp8_sdwa v[98:99], v118 src0_sel:WORD_1
	v_cvt_pk_f32_fp8_e32 v[96:97], v118
	v_pk_add_f32 v[94:95], v[94:95], 0 op_sel_hi:[1,0]
	v_pk_add_f32 v[92:93], v[92:93], 0 op_sel_hi:[1,0]
	v_cvt_pk_f32_fp8_e32 v[100:101], v120
	v_pk_add_f32 v[92:93], v[92:93], v[98:99]
	v_cvt_pk_f32_fp8_e32 v[98:99], v119
	v_pk_add_f32 v[94:95], v[94:95], v[96:97]
	v_cvt_pk_f32_fp8_sdwa v[96:97], v119 src0_sel:WORD_1
	v_cvt_pk_f32_fp8_sdwa v[102:103], v120 src0_sel:WORD_1
	v_pk_add_f32 v[94:95], v[94:95], v[98:99]
	s_add_u32 s14, s0, s14
	v_pk_add_f32 v[94:95], v[94:95], v[100:101]
	v_pk_add_f32 v[92:93], v[92:93], v[96:97]
	v_pk_mul_f32 v[94:95], v[94:95], s[8:9] op_sel_hi:[1,0]
	v_pk_add_f32 v[92:93], v[92:93], v[102:103]
	v_mul_f32_e32 v96, v95, v95
	v_pk_mul_f32 v[92:93], v[92:93], s[8:9] op_sel_hi:[1,0]
	v_fmac_f32_e32 v96, v94, v94
	v_fmac_f32_e32 v96, v92, v92
	v_fmac_f32_e32 v96, v93, v93
	v_add_f32_e32 v96, v104, v96
	s_addc_u32 s15, s1, s15
	v_lshlrev_b32_e32 v102, 16, v62
	v_add_f32_dpp v96, v96, v96 quad_perm:[1,0,3,2] row_mask:0xf bank_mask:0xf bound_ctrl:1
	v_and_b32_e32 v103, 0xffff0000, v62
	v_lshlrev_b32_e32 v62, 16, v63
	v_add_f32_dpp v96, v96, v96 quad_perm:[2,3,0,1] row_mask:0xf bank_mask:0xf bound_ctrl:1
	v_and_b32_e32 v63, 0xffff0000, v63
	s_add_i32 s2, s2, s48
	v_add_f32_dpp v96, v96, v96 row_half_mirror row_mask:0xf bank_mask:0xf bound_ctrl:1
	v_lshl_add_u64 v[42:43], v[42:43], 0, s[4:5]
	v_lshl_add_u64 v[44:45], v[44:45], 0, s[6:7]
	v_add_f32_dpp v96, v96, v96 row_mirror row_mask:0xf bank_mask:0xf bound_ctrl:1
	v_mov_b32_e32 v97, v96
	s_nop 1
	v_permlane16_swap_b32_e32 v96, v97
	v_add_f32_e32 v96, v96, v97
	v_mov_b32_e32 v97, v96
	s_nop 1
	v_permlane32_swap_b32_e32 v96, v97
	v_add_f32_e32 v96, v96, v97
	v_fmamk_f32 v96, v96, 0x3a000000, v116
	v_mul_f32_e32 v97, 0x4b800000, v96
	v_cmp_gt_f32_e32 vcc, s22, v96
	s_cmpk_gt_i32 s2, 0xff
	v_lshl_add_u64 v[46:47], v[46:47], 0, s[4:5]
	v_cndmask_b32_e32 v96, v96, v97, vcc
	v_rsq_f32_e32 v100, v96
	v_lshl_add_u64 v[96:97], s[14:15], 0, v[36:37]
	v_lshl_add_u64 v[98:99], v[96:97], 0, s[12:13]
	v_mul_f32_e32 v101, 0x45800000, v100
	v_cndmask_b32_e32 v100, v100, v101, vcc
	v_pk_mul_f32 v[64:65], v[64:65], v[100:101] op_sel_hi:[1,0]
	v_pk_mul_f32 v[66:67], v[66:67], v[100:101] op_sel_hi:[1,0]
	v_pk_fma_f32 v[30:31], v[30:31], v[64:65], v[62:63]
	v_add_co_u32_e32 v62, vcc, s23, v96
	v_pk_fma_f32 v[28:29], v[28:29], v[66:67], v[102:103]
	s_nop 0
	v_addc_co_u32_e32 v63, vcc, 0, v97, vcc
	global_store_dwordx4 v[62:63], v[28:31], off offset:-4096 nt
	s_waitcnt vmcnt(15)
	s_nop 0
	v_lshlrev_b32_e32 v28, 16, v60
	v_and_b32_e32 v29, 0xffff0000, v60
	v_pk_mul_f32 v[30:31], v[70:71], v[100:101] op_sel_hi:[1,0]
	s_nop 0
	v_pk_fma_f32 v[24:25], v[24:25], v[30:31], v[28:29]
	v_lshlrev_b32_e32 v28, 16, v61
	v_and_b32_e32 v29, 0xffff0000, v61
	v_pk_mul_f32 v[30:31], v[68:69], v[100:101] op_sel_hi:[1,0]
	s_nop 0
	v_pk_fma_f32 v[26:27], v[26:27], v[30:31], v[28:29]
	global_store_dwordx4 v[98:99], v[24:27], off offset:1024 nt
	s_waitcnt vmcnt(15)
	s_nop 0
	v_lshlrev_b32_e32 v24, 16, v58
	v_and_b32_e32 v25, 0xffff0000, v58
	v_pk_mul_f32 v[26:27], v[74:75], v[100:101] op_sel_hi:[1,0]
	s_nop 0
	v_pk_fma_f32 v[20:21], v[20:21], v[26:27], v[24:25]
	v_lshlrev_b32_e32 v24, 16, v59
	v_and_b32_e32 v25, 0xffff0000, v59
	v_pk_mul_f32 v[26:27], v[72:73], v[100:101] op_sel_hi:[1,0]
	s_nop 0
	v_pk_fma_f32 v[22:23], v[22:23], v[26:27], v[24:25]
	global_store_dwordx4 v[98:99], v[20:23], off offset:2048 nt
	s_waitcnt vmcnt(15)
	s_nop 0
	v_lshlrev_b32_e32 v20, 16, v56
	v_and_b32_e32 v21, 0xffff0000, v56
	v_pk_mul_f32 v[22:23], v[78:79], v[100:101] op_sel_hi:[1,0]
	s_nop 0
	v_pk_fma_f32 v[16:17], v[16:17], v[22:23], v[20:21]
	v_lshlrev_b32_e32 v20, 16, v57
	v_and_b32_e32 v21, 0xffff0000, v57
	v_pk_mul_f32 v[22:23], v[76:77], v[100:101] op_sel_hi:[1,0]
	s_nop 0
	v_pk_fma_f32 v[18:19], v[18:19], v[22:23], v[20:21]
	global_store_dwordx4 v[98:99], v[16:19], off offset:3072 nt
	s_waitcnt vmcnt(15)
	s_nop 0
	v_lshlrev_b32_e32 v16, 16, v54
	v_and_b32_e32 v17, 0xffff0000, v54
	v_pk_mul_f32 v[18:19], v[82:83], v[100:101] op_sel_hi:[1,0]
	s_nop 0
	v_pk_fma_f32 v[12:13], v[12:13], v[18:19], v[16:17]
	v_lshlrev_b32_e32 v16, 16, v55
	v_and_b32_e32 v17, 0xffff0000, v55
	v_pk_mul_f32 v[18:19], v[80:81], v[100:101] op_sel_hi:[1,0]
	s_nop 0
	v_pk_fma_f32 v[14:15], v[14:15], v[18:19], v[16:17]
	global_store_dwordx4 v[62:63], v[12:15], off nt
	s_waitcnt vmcnt(15)
	s_nop 0
	v_lshlrev_b32_e32 v12, 16, v52
	v_and_b32_e32 v13, 0xffff0000, v52
	v_pk_mul_f32 v[14:15], v[86:87], v[100:101] op_sel_hi:[1,0]
	s_nop 0
	v_pk_fma_f32 v[8:9], v[8:9], v[14:15], v[12:13]
	v_lshlrev_b32_e32 v12, 16, v53
	v_and_b32_e32 v13, 0xffff0000, v53
	v_pk_mul_f32 v[14:15], v[84:85], v[100:101] op_sel_hi:[1,0]
	s_nop 0
	v_pk_fma_f32 v[10:11], v[10:11], v[14:15], v[12:13]
	global_store_dwordx4 v[62:63], v[8:11], off offset:1024 nt
	s_waitcnt vmcnt(15)
	s_nop 0
	v_lshlrev_b32_e32 v8, 16, v50
	v_and_b32_e32 v9, 0xffff0000, v50
	v_pk_mul_f32 v[10:11], v[90:91], v[100:101] op_sel_hi:[1,0]
	s_nop 0
	v_pk_fma_f32 v[4:5], v[4:5], v[10:11], v[8:9]
	v_lshlrev_b32_e32 v8, 16, v51
	v_and_b32_e32 v9, 0xffff0000, v51
	v_pk_mul_f32 v[10:11], v[88:89], v[100:101] op_sel_hi:[1,0]
	s_nop 0
	v_pk_fma_f32 v[6:7], v[6:7], v[10:11], v[8:9]
	global_store_dwordx4 v[62:63], v[4:7], off offset:2048 nt
	s_waitcnt vmcnt(15)
	s_nop 0
	v_lshlrev_b32_e32 v4, 16, v48
	v_and_b32_e32 v5, 0xffff0000, v48
	v_pk_mul_f32 v[6:7], v[94:95], v[100:101] op_sel_hi:[1,0]
	s_nop 0
	v_pk_fma_f32 v[0:1], v[0:1], v[6:7], v[4:5]
	v_lshlrev_b32_e32 v4, 16, v49
	v_and_b32_e32 v5, 0xffff0000, v49
	v_pk_mul_f32 v[6:7], v[92:93], v[100:101] op_sel_hi:[1,0]
	s_nop 0
	v_pk_fma_f32 v[2:3], v[2:3], v[6:7], v[4:5]
	global_store_dwordx4 v[62:63], v[0:3], off offset:3072 nt
	s_cbranch_scc0 .LBB0_2518
